# MLA MFMA streams at priority 1 with brief priority drops every 8 MFMAs (GEMM-template style)
# speedup vs baseline: 1.0053x; 1.0013x over previous
.Lb2:
	s_setprio 1
	s_add_i32 s14, s10, -2
	s_and_b32 s14, s14, 3
	s_mulk_i32 s14, 0x6000
	v_add_u32_e32 v146, s14, v147
	v_add_u32_e32 v161, s14, v148
	v_add_u32_e32 v144, s14, v149
	v_add_u32_e32 v168, s14, v150
	s_waitcnt lgkmcnt(14)
	v_mfma_f32_32x32x16_bf16 v[48:63], v[224:227], v[76:79], v[48:63]
	ds_read_b64_tr_b16 v[224:225], v166
	ds_read_b64_tr_b16 v[226:227], v167 offset:768
	s_waitcnt lgkmcnt(14)
	v_mfma_f32_32x32x16_bf16 v[0:15], v[228:231], v[76:79], v[0:15]
	ds_read_b64_tr_b16 v[228:229], v166 offset:128
	ds_read_b64_tr_b16 v[230:231], v167 offset:896
	s_waitcnt lgkmcnt(14)
	v_mfma_f32_32x32x16_bf16 v[48:63], v[232:235], v[72:75], v[48:63]
	ds_read_b64_tr_b16 v[232:233], v166 offset:6144
	ds_read_b64_tr_b16 v[234:235], v167 offset:6912
	s_waitcnt lgkmcnt(14)
	v_mfma_f32_32x32x16_bf16 v[0:15], v[236:239], v[72:75], v[0:15]
	ds_read_b64_tr_b16 v[236:237], v166 offset:6272
	ds_read_b64_tr_b16 v[238:239], v167 offset:7040
	s_waitcnt lgkmcnt(14)
	v_mfma_f32_32x32x16_bf16 v[48:63], v[240:243], v[64:67], v[48:63]
	ds_read_b64_tr_b16 v[240:241], v166 offset:12288
	ds_read_b64_tr_b16 v[242:243], v167 offset:13056
	s_waitcnt lgkmcnt(14)
	v_mfma_f32_32x32x16_bf16 v[0:15], v[244:247], v[64:67], v[0:15]
	ds_read_b64_tr_b16 v[244:245], v166 offset:12416
	ds_read_b64_tr_b16 v[246:247], v167 offset:13184
	s_waitcnt lgkmcnt(14)
	v_mfma_f32_32x32x16_bf16 v[48:63], v[252:255], v[68:71], v[48:63]
	ds_read_b64_tr_b16 v[252:253], v166 offset:18432
	ds_read_b64_tr_b16 v[254:255], v167 offset:19200
	s_waitcnt lgkmcnt(14)
	v_mfma_f32_32x32x16_bf16 v[0:15], v[204:207], v[68:71], v[0:15]
	s_setprio 0
	s_setprio 1
	ds_read_b64_tr_b16 v[204:205], v166 offset:18560
	ds_read_b64_tr_b16 v[206:207], v167 offset:19328
	s_waitcnt lgkmcnt(14)
	v_mfma_f32_32x32x16_bf16 v[32:47], v[224:227], v[76:79], v[32:47]
	ds_read_b128 v[224:227], v146
	s_waitcnt lgkmcnt(13)
	v_mfma_f32_32x32x16_bf16 v[16:31], v[228:231], v[76:79], v[16:31]
	ds_read_b128 v[228:231], v146 offset:12288
	s_waitcnt lgkmcnt(12)
	v_mfma_f32_32x32x16_bf16 v[32:47], v[232:235], v[72:75], v[32:47]
	ds_read_b128 v[232:235], v161
	s_waitcnt lgkmcnt(11)
	v_mfma_f32_32x32x16_bf16 v[16:31], v[236:239], v[72:75], v[16:31]
	ds_read_b128 v[236:239], v161 offset:12288
	s_waitcnt lgkmcnt(10)
	v_mfma_f32_32x32x16_bf16 v[32:47], v[240:243], v[64:67], v[32:47]
	ds_read_b128 v[240:243], v144
	s_waitcnt lgkmcnt(9)
	v_mfma_f32_32x32x16_bf16 v[16:31], v[244:247], v[64:67], v[16:31]
	ds_read_b128 v[244:247], v144 offset:12288
	s_waitcnt lgkmcnt(8)
	v_mfma_f32_32x32x16_bf16 v[32:47], v[252:255], v[68:71], v[32:47]
	ds_read_b128 v[252:255], v168
	s_waitcnt lgkmcnt(7)
	v_mfma_f32_32x32x16_bf16 v[16:31], v[204:207], v[68:71], v[16:31]
	s_setprio 0
	s_setprio 1
	ds_read_b128 v[204:207], v168 offset:12288
	s_waitcnt lgkmcnt(7)
	v_mfma_f32_32x32x16_bf16 v[80:95], v[224:227], v[112:115], 0
	ds_read_b128 v[224:227], v146 offset:128
	s_waitcnt lgkmcnt(7)
	v_mfma_f32_32x32x16_bf16 v[64:79], v[228:231], v[112:115], 0
	ds_read_b128 v[228:231], v146 offset:12416
	s_waitcnt lgkmcnt(7)
	v_mfma_f32_32x32x16_bf16 v[80:95], v[232:235], v[116:119], v[80:95]
	ds_read_b128 v[232:235], v161 offset:128
	s_waitcnt lgkmcnt(7)
	v_mfma_f32_32x32x16_bf16 v[64:79], v[236:239], v[116:119], v[64:79]
	ds_read_b128 v[236:239], v161 offset:12416
	s_waitcnt lgkmcnt(7)
	v_mfma_f32_32x32x16_bf16 v[80:95], v[240:243], v[120:123], v[80:95]
	ds_read_b128 v[240:243], v144 offset:128
	s_waitcnt lgkmcnt(7)
	v_mfma_f32_32x32x16_bf16 v[64:79], v[244:247], v[120:123], v[64:79]
	ds_read_b128 v[244:247], v144 offset:12416
	s_waitcnt lgkmcnt(7)
	v_mfma_f32_32x32x16_bf16 v[80:95], v[252:255], v[124:127], v[80:95]
	ds_read_b128 v[252:255], v168 offset:128
	s_waitcnt lgkmcnt(7)
	v_mfma_f32_32x32x16_bf16 v[64:79], v[204:207], v[124:127], v[64:79]
	s_setprio 0
	s_setprio 1
	ds_read_b128 v[204:207], v168 offset:12416
	s_waitcnt lgkmcnt(7)
	v_mfma_f32_32x32x16_bf16 v[80:95], v[224:227], v[96:99], v[80:95]
	ds_read_b128 v[224:227], v146 offset:256
	s_waitcnt lgkmcnt(7)
	v_mfma_f32_32x32x16_bf16 v[64:79], v[228:231], v[96:99], v[64:79]
	ds_read_b128 v[228:231], v146 offset:12544
	s_waitcnt lgkmcnt(7)
	v_mfma_f32_32x32x16_bf16 v[80:95], v[232:235], v[100:103], v[80:95]
	ds_read_b128 v[232:235], v161 offset:256
	s_waitcnt lgkmcnt(7)
	v_mfma_f32_32x32x16_bf16 v[64:79], v[236:239], v[100:103], v[64:79]
	ds_read_b128 v[236:239], v161 offset:12544
	s_waitcnt lgkmcnt(7)
	v_mfma_f32_32x32x16_bf16 v[80:95], v[240:243], v[104:107], v[80:95]
	ds_read_b128 v[240:243], v144 offset:256
	s_waitcnt lgkmcnt(7)
	v_mfma_f32_32x32x16_bf16 v[64:79], v[244:247], v[104:107], v[64:79]
	ds_read_b128 v[244:247], v144 offset:12544
	s_waitcnt lgkmcnt(7)
	v_mfma_f32_32x32x16_bf16 v[80:95], v[252:255], v[108:111], v[80:95]
	ds_read_b128 v[252:255], v168 offset:256
	s_waitcnt lgkmcnt(7)
	v_mfma_f32_32x32x16_bf16 v[64:79], v[204:207], v[108:111], v[64:79]
	s_setprio 0
	s_setprio 1
	ds_read_b128 v[204:207], v168 offset:12544
	s_waitcnt lgkmcnt(7)
	v_mfma_f32_32x32x16_bf16 v[80:95], v[224:227], v[128:131], v[80:95]
	s_waitcnt lgkmcnt(6)
	v_mfma_f32_32x32x16_bf16 v[64:79], v[228:231], v[128:131], v[64:79]
	s_waitcnt lgkmcnt(5)
	v_mfma_f32_32x32x16_bf16 v[80:95], v[232:235], v[132:135], v[80:95]
	s_waitcnt lgkmcnt(4)
	v_mfma_f32_32x32x16_bf16 v[64:79], v[236:239], v[132:135], v[64:79]
	s_waitcnt lgkmcnt(3)
	v_mfma_f32_32x32x16_bf16 v[80:95], v[240:243], v[136:139], v[80:95]
	s_waitcnt lgkmcnt(2)
	v_mfma_f32_32x32x16_bf16 v[64:79], v[244:247], v[136:139], v[64:79]
	s_waitcnt lgkmcnt(1)
	v_mfma_f32_32x32x16_bf16 v[80:95], v[252:255], v[140:143], v[80:95]
	s_waitcnt lgkmcnt(0)
	v_mfma_f32_32x32x16_bf16 v[64:79], v[204:207], v[140:143], v[64:79]
	s_setprio 0
	s_waitcnt vmcnt(0)
	s_cmp_lt_u32 s88, 0x1000
	s_cbranch_scc1 .Lb3
	s_barrier

.Lb4:
	s_cmp_ge_u32 s13, s9
	s_setprio 1
	v_add_u32_e32 v144, s98, v147
	v_add_u32_e32 v146, s98, v148
	v_add_u32_e32 v161, s98, v149
	v_add_u32_e32 v168, s98, v150
	s_waitcnt lgkmcnt(14)
	v_mfma_f32_32x32x16_bf16 v[48:63], v[224:227], v[72:75], v[48:63]
	ds_read_b64_tr_b16 v[224:225], v213
	ds_read_b64_tr_b16 v[226:227], v214 offset:768
	s_waitcnt lgkmcnt(14)
	v_mfma_f32_32x32x16_bf16 v[0:15], v[228:231], v[72:75], v[0:15]
	ds_read_b64_tr_b16 v[228:229], v213 offset:128
	ds_read_b64_tr_b16 v[230:231], v214 offset:896
	s_waitcnt lgkmcnt(14)
	v_mfma_f32_32x32x16_bf16 v[48:63], v[232:235], v[76:79], v[48:63]
	ds_read_b64_tr_b16 v[232:233], v213 offset:6144
	ds_read_b64_tr_b16 v[234:235], v214 offset:6912
	s_waitcnt lgkmcnt(14)
	v_mfma_f32_32x32x16_bf16 v[0:15], v[236:239], v[76:79], v[0:15]
	ds_read_b64_tr_b16 v[236:237], v213 offset:6272
	ds_read_b64_tr_b16 v[238:239], v214 offset:7040
	s_waitcnt lgkmcnt(14)
	v_mfma_f32_32x32x16_bf16 v[48:63], v[240:243], v[68:71], v[48:63]
	ds_read_b64_tr_b16 v[240:241], v213 offset:12288
	ds_read_b64_tr_b16 v[242:243], v214 offset:13056
	s_waitcnt lgkmcnt(14)
	v_mfma_f32_32x32x16_bf16 v[0:15], v[244:247], v[68:71], v[0:15]
	ds_read_b64_tr_b16 v[244:245], v213 offset:12416
	ds_read_b64_tr_b16 v[246:247], v214 offset:13184
	s_waitcnt lgkmcnt(14)
	v_mfma_f32_32x32x16_bf16 v[48:63], v[252:255], v[64:67], v[48:63]
	ds_read_b64_tr_b16 v[252:253], v213 offset:18432
	ds_read_b64_tr_b16 v[254:255], v214 offset:19200
	s_waitcnt lgkmcnt(14)
	v_mfma_f32_32x32x16_bf16 v[0:15], v[204:207], v[64:67], v[0:15]
	s_setprio 0
	s_setprio 1
	ds_read_b64_tr_b16 v[204:205], v213 offset:18560
	ds_read_b64_tr_b16 v[206:207], v214 offset:19328
	s_waitcnt lgkmcnt(14)
	v_mfma_f32_32x32x16_bf16 v[32:47], v[224:227], v[72:75], v[32:47]
	ds_read_b128 v[224:227], v144
	s_waitcnt lgkmcnt(13)
	v_mfma_f32_32x32x16_bf16 v[16:31], v[228:231], v[72:75], v[16:31]
	ds_read_b128 v[228:231], v144 offset:12288
	s_waitcnt lgkmcnt(12)
	v_mfma_f32_32x32x16_bf16 v[32:47], v[232:235], v[76:79], v[32:47]
	ds_read_b128 v[232:235], v146
	s_waitcnt lgkmcnt(11)
	v_mfma_f32_32x32x16_bf16 v[16:31], v[236:239], v[76:79], v[16:31]
	ds_read_b128 v[236:239], v146 offset:12288
	s_waitcnt lgkmcnt(10)
	v_mfma_f32_32x32x16_bf16 v[32:47], v[240:243], v[68:71], v[32:47]
	ds_read_b128 v[240:243], v161
	s_waitcnt lgkmcnt(9)
	v_mfma_f32_32x32x16_bf16 v[16:31], v[244:247], v[68:71], v[16:31]
	ds_read_b128 v[244:247], v161 offset:12288
	s_waitcnt lgkmcnt(8)
	v_mfma_f32_32x32x16_bf16 v[32:47], v[252:255], v[64:67], v[32:47]
	ds_read_b128 v[252:255], v168
	s_waitcnt lgkmcnt(7)
	v_mfma_f32_32x32x16_bf16 v[16:31], v[204:207], v[64:67], v[16:31]
	s_setprio 0
	s_setprio 1
	ds_read_b128 v[204:207], v168 offset:12288
	s_cbranch_scc1 .LBB0_1250
	s_add_i32 s13, s10, -1
	s_mov_b32 s14, s98
	s_waitcnt lgkmcnt(7)
	v_mfma_f32_32x32x16_bf16 v[80:95], v[224:227], v[112:115], 0
	ds_read_b128 v[224:227], v144 offset:128
	s_waitcnt lgkmcnt(7)
	v_mfma_f32_32x32x16_bf16 v[64:79], v[228:231], v[112:115], 0
	ds_read_b128 v[228:231], v144 offset:12416
	s_waitcnt lgkmcnt(7)
	v_mfma_f32_32x32x16_bf16 v[80:95], v[232:235], v[116:119], v[80:95]
	ds_read_b128 v[232:235], v146 offset:128
	s_waitcnt lgkmcnt(7)
	v_mfma_f32_32x32x16_bf16 v[64:79], v[236:239], v[116:119], v[64:79]
	ds_read_b128 v[236:239], v146 offset:12416
	s_waitcnt lgkmcnt(7)
	v_mfma_f32_32x32x16_bf16 v[80:95], v[240:243], v[120:123], v[80:95]
	ds_read_b128 v[240:243], v161 offset:128
	s_waitcnt lgkmcnt(7)
	v_mfma_f32_32x32x16_bf16 v[64:79], v[244:247], v[120:123], v[64:79]
	ds_read_b128 v[244:247], v161 offset:12416
	s_waitcnt lgkmcnt(7)
	v_mfma_f32_32x32x16_bf16 v[80:95], v[252:255], v[124:127], v[80:95]
	ds_read_b128 v[252:255], v168 offset:128
	s_waitcnt lgkmcnt(7)
	v_mfma_f32_32x32x16_bf16 v[64:79], v[204:207], v[124:127], v[64:79]
	s_setprio 0
	s_setprio 1
	ds_read_b128 v[204:207], v168 offset:12416
	s_waitcnt lgkmcnt(7)
	v_mfma_f32_32x32x16_bf16 v[80:95], v[224:227], v[96:99], v[80:95]
	ds_read_b128 v[224:227], v144 offset:256
	s_waitcnt lgkmcnt(7)
	v_mfma_f32_32x32x16_bf16 v[64:79], v[228:231], v[96:99], v[64:79]
	ds_read_b128 v[228:231], v144 offset:12544
	s_waitcnt lgkmcnt(7)
	v_mfma_f32_32x32x16_bf16 v[80:95], v[232:235], v[100:103], v[80:95]
	ds_read_b128 v[232:235], v146 offset:256
	s_waitcnt lgkmcnt(7)
	v_mfma_f32_32x32x16_bf16 v[64:79], v[236:239], v[100:103], v[64:79]
	ds_read_b128 v[236:239], v146 offset:12544
	s_waitcnt lgkmcnt(7)
	v_mfma_f32_32x32x16_bf16 v[80:95], v[240:243], v[104:107], v[80:95]
	ds_read_b128 v[240:243], v161 offset:256
	s_waitcnt lgkmcnt(7)
	v_mfma_f32_32x32x16_bf16 v[64:79], v[244:247], v[104:107], v[64:79]
	ds_read_b128 v[244:247], v161 offset:12544
	s_waitcnt lgkmcnt(7)
	v_mfma_f32_32x32x16_bf16 v[80:95], v[252:255], v[108:111], v[80:95]
	ds_read_b128 v[252:255], v168 offset:256
	s_waitcnt lgkmcnt(7)
	v_mfma_f32_32x32x16_bf16 v[64:79], v[204:207], v[108:111], v[64:79]
	s_setprio 0
	s_setprio 1
	ds_read_b128 v[204:207], v168 offset:12544
	s_waitcnt lgkmcnt(7)
	v_mfma_f32_32x32x16_bf16 v[80:95], v[224:227], v[128:131], v[80:95]
	s_waitcnt lgkmcnt(6)
	v_mfma_f32_32x32x16_bf16 v[64:79], v[228:231], v[128:131], v[64:79]
	s_waitcnt lgkmcnt(5)
	v_mfma_f32_32x32x16_bf16 v[80:95], v[232:235], v[132:135], v[80:95]
	s_waitcnt lgkmcnt(4)
	v_mfma_f32_32x32x16_bf16 v[64:79], v[236:239], v[132:135], v[64:79]
	s_waitcnt lgkmcnt(3)
	v_mfma_f32_32x32x16_bf16 v[80:95], v[240:243], v[136:139], v[80:95]
	s_waitcnt lgkmcnt(2)
	v_mfma_f32_32x32x16_bf16 v[64:79], v[244:247], v[136:139], v[64:79]
	s_waitcnt lgkmcnt(1)
	v_mfma_f32_32x32x16_bf16 v[80:95], v[252:255], v[140:143], v[80:95]
	s_waitcnt lgkmcnt(0)
	v_mfma_f32_32x32x16_bf16 v[64:79], v[204:207], v[140:143], v[64:79]
	s_setprio 0
	s_waitcnt vmcnt(0)
	s_cmp_lt_u32 s88, 0x1000
	s_cbranch_scc1 .Lb1
	s_barrier

.LBB0_1250:
	s_setprio 0
	s_waitcnt vmcnt(0) lgkmcnt(0)
